# code placement: phase-12 loop head moved 48 bytes (to 0x20 mod 64) with s_nop padding
# speedup vs baseline: 1.0010x; 1.0010x over previous
.Lv_reprime:
	s_lshl_b32 s2, s20, 8
	s_add_u32 s2, s28, s2
	s_addc_u32 s3, s29, 0
	global_load_dwordx4 v[8:11], v2, s[2:3]
	global_load_dwordx4 v[12:15], v2, s[2:3] offset:16
	s_lshl_b32 s2, s20, 8
	s_add_u32 s2, s30, s2
	s_addc_u32 s3, s31, 0
	global_load_dwordx4 v[24:27], v2, s[2:3]
	global_load_dwordx4 v[28:31], v2, s[2:3] offset:16
	s_lshl_b32 s2, s21, 8
	s_add_u32 s2, s28, s2
	s_addc_u32 s3, s29, 0
	global_load_dwordx4 v[16:19], v2, s[2:3]
	global_load_dwordx4 v[20:23], v2, s[2:3] offset:16
	s_waitcnt vmcnt(0)
	v_mad_u32_u16 v112, v8, s46, v1
	buffer_load_dwordx4 v[48:51], v112, s[36:39], 0 offen
	v_mad_u32_u16 v113, v8, s46, v1 op_sel:[1,0,0,0]
	buffer_load_dwordx4 v[52:55], v113, s[36:39], 0 offen
	v_mad_u32_u16 v112, v9, s46, v1
	buffer_load_dwordx4 v[56:59], v112, s[36:39], 0 offen
	v_mad_u32_u16 v113, v9, s46, v1 op_sel:[1,0,0,0]
	buffer_load_dwordx4 v[60:63], v113, s[36:39], 0 offen
	v_mad_u32_u16 v112, v10, s46, v1
	buffer_load_dwordx4 v[64:67], v112, s[36:39], 0 offen
	v_mad_u32_u16 v113, v10, s46, v1 op_sel:[1,0,0,0]
	buffer_load_dwordx4 v[68:71], v113, s[36:39], 0 offen
	v_mad_u32_u16 v112, v11, s46, v1
	buffer_load_dwordx4 v[72:75], v112, s[36:39], 0 offen
	v_mad_u32_u16 v113, v11, s46, v1 op_sel:[1,0,0,0]
	buffer_load_dwordx4 v[76:79], v113, s[36:39], 0 offen
	v_mad_u32_u16 v112, v12, s46, v1
	buffer_load_dwordx4 v[80:83], v112, s[36:39], 0 offen
	v_mad_u32_u16 v113, v12, s46, v1 op_sel:[1,0,0,0]
	buffer_load_dwordx4 v[84:87], v113, s[36:39], 0 offen
	v_mad_u32_u16 v112, v13, s46, v1
	buffer_load_dwordx4 v[88:91], v112, s[36:39], 0 offen
	v_mad_u32_u16 v113, v13, s46, v1 op_sel:[1,0,0,0]
	buffer_load_dwordx4 v[92:95], v113, s[36:39], 0 offen
	v_mad_u32_u16 v112, v14, s46, v1
	buffer_load_dwordx4 v[96:99], v112, s[36:39], 0 offen
	v_mad_u32_u16 v113, v14, s46, v1 op_sel:[1,0,0,0]
	buffer_load_dwordx4 v[100:103], v113, s[36:39], 0 offen
	v_mad_u32_u16 v112, v15, s46, v1
	buffer_load_dwordx4 v[104:107], v112, s[36:39], 0 offen
	v_mad_u32_u16 v113, v15, s46, v1 op_sel:[1,0,0,0]
	buffer_load_dwordx4 v[108:111], v113, s[36:39], 0 offen
	global_load_dword v252, v5, s[28:29]
	s_nop 0
	s_nop 0
	s_nop 0
	s_nop 0
	s_nop 0
	s_nop 0
	s_nop 0
	s_nop 0
	s_nop 0
	s_nop 0
	s_nop 0
	s_nop 0

.Lv_next_slice:
	s_waitcnt vmcnt(0)
	s_add_u32 s17, s17, 1
	s_add_u32 s16, s16, 1
	s_cmp_lt_u32 s17, 2
	s_cbranch_scc1 .Lv_slice
	s_nop 0
	s_nop 0
	s_nop 0
	s_nop 0
